# E24: E23 + gla_c epilogue norm-weight loads rotated through three free register quads so each is issued three steps ahead (counted vmcnt waits instead of load/vmcnt(0)/store chain)
# baseline (speedup 1.0000x reference)
.LBB0_903:
	s_or_b64 exec, exec, s[0:1]
	s_waitcnt lgkmcnt(0)
	s_barrier
	global_load_dwordx4 v[72:75], v[84:85], off
	global_load_dwordx4 v[240:243], v[86:87], off
	global_load_dwordx4 v[244:247], v[88:89], off
	global_load_dwordx4 v[248:251], v[90:91], off
	ds_read2st64_b32 v[76:77], v149 offset1:1
	v_lshlrev_b32_e32 v78, 16, v130
	v_and_b32_e32 v81, 0xffff0000, v131
	v_and_b32_e32 v79, 0xffff0000, v130
	v_mul_f32_e32 v0, 0xbfb8aa3b, v78
	v_mul_f32_e32 v130, 0xbfb8aa3b, v81
	v_mul_f32_e32 v70, 0xbfb8aa3b, v79
	v_exp_f32_e32 v0, v0
	v_exp_f32_e32 v130, v130
	v_exp_f32_e32 v70, v70
	s_waitcnt lgkmcnt(0)
	v_add_f32_e32 v76, v76, v77
	v_lshlrev_b32_e32 v80, 16, v131
	v_fmamk_f32 v131, v76, 0x3b800000, v190
	s_mov_b32 s0, 0xf800000
	v_add_f32_e32 v0, 1.0, v0
	v_add_f32_e32 v211, 1.0, v130
	v_mul_f32_e32 v130, 0x4f800000, v131
	v_cmp_gt_f32_e32 vcc, s0, v131
	v_mul_f32_e32 v82, 0xbfb8aa3b, v80
	v_add_f32_e32 v70, 1.0, v70
	v_rcp_f32_e32 v76, v0
	v_cndmask_b32_e32 v0, v131, v130, vcc
	v_exp_f32_e32 v82, v82
	v_rcp_f32_e32 v77, v70
	v_sqrt_f32_e32 v70, v0
	v_rcp_f32_e32 v131, v211
	v_add_f32_e32 v82, 1.0, v82
	v_pk_mul_f32 v[76:77], v[76:77], v[78:79]
	v_add_u32_e32 v78, -1, v70
	v_rcp_f32_e32 v130, v82
	v_add_u32_e32 v79, 1, v70
	v_fma_f32 v82, -v78, v70, v0
	v_fma_f32 v211, -v79, v70, v0
	v_cmp_ge_f32_e64 s[0:1], 0, v82
	v_lshl_or_b32 v71, s37, 8, v210
	v_add_lshl_u32 v210, v71, v150, 1
	v_cndmask_b32_e64 v70, v70, v78, s[0:1]
	v_cmp_lt_f32_e64 s[0:1], 0, v211
	s_add_u32 s68, s68, s70
	s_addc_u32 s69, s69, s71
	v_cndmask_b32_e64 v70, v70, v79, s[0:1]
	v_mul_f32_e32 v78, 0x37800000, v70
	v_cndmask_b32_e32 v70, v70, v78, vcc
	v_cmp_class_f32_e32 vcc, v0, v191
	v_pk_mul_f32 v[78:79], v[130:131], v[80:81]
	s_add_i32 s36, s36, s79
	v_cndmask_b32_e32 v0, v70, v0, vcc
	v_div_scale_f32 v70, s[0:1], v0, v0, 1.0
	v_rcp_f32_e32 v82, v70
	v_div_scale_f32 v80, vcc, 1.0, v0, 1.0
	s_add_i32 s33, s33, s80
	v_fma_f32 v81, -v70, v82, 1.0
	v_fmac_f32_e32 v82, v81, v82
	v_mul_f32_e32 v81, v80, v82
	v_fma_f32 v130, -v70, v81, v80
	v_fmac_f32_e32 v81, v130, v82
	v_fma_f32 v70, -v70, v81, v80
	v_div_fmas_f32 v70, v70, v82, v81
	v_div_fixup_f32 v70, v70, v0, 1.0
	v_pk_mul_f32 v[66:67], v[66:67], v[70:71] op_sel_hi:[1,0]
	v_pk_mul_f32 v[68:69], v[68:69], v[70:71] op_sel_hi:[1,0]
	v_pk_mul_f32 v[62:63], v[62:63], v[70:71] op_sel_hi:[1,0]
	v_pk_mul_f32 v[64:65], v[64:65], v[70:71] op_sel_hi:[1,0]
	v_pk_mul_f32 v[58:59], v[58:59], v[70:71] op_sel_hi:[1,0]
	v_pk_mul_f32 v[60:61], v[60:61], v[70:71] op_sel_hi:[1,0]
	v_pk_mul_f32 v[54:55], v[54:55], v[70:71] op_sel_hi:[1,0]
	v_pk_mul_f32 v[56:57], v[56:57], v[70:71] op_sel_hi:[1,0]
	v_pk_mul_f32 v[50:51], v[50:51], v[70:71] op_sel_hi:[1,0]
	v_pk_mul_f32 v[52:53], v[52:53], v[70:71] op_sel_hi:[1,0]
	v_pk_mul_f32 v[46:47], v[46:47], v[70:71] op_sel_hi:[1,0]
	v_pk_mul_f32 v[48:49], v[48:49], v[70:71] op_sel_hi:[1,0]
	v_pk_mul_f32 v[42:43], v[42:43], v[70:71] op_sel_hi:[1,0]
	v_pk_mul_f32 v[44:45], v[44:45], v[70:71] op_sel_hi:[1,0]
	v_pk_mul_f32 v[38:39], v[38:39], v[70:71] op_sel_hi:[1,0]
	v_pk_mul_f32 v[40:41], v[40:41], v[70:71] op_sel_hi:[1,0]
	s_andn2_b64 vcc, exec, s[72:73]
	s_mov_b32 s96, s97
	s_waitcnt vmcnt(3)
	v_pk_mul_f32 v[66:67], v[72:73], v[66:67]
	v_pk_mul_f32 v[68:69], v[74:75], v[68:69]
	v_pk_mul_f32 v[66:67], v[76:77], v[66:67]
	v_pk_mul_f32 v[68:69], v[78:79], v[68:69]
	v_cvt_pk_bf16_f32 v66, v66, v67
	v_cvt_pk_bf16_f32 v67, v68, v69
	global_store_dwordx2 v210, v[66:67], s[24:25]
	v_lshlrev_b32_e32 v72, 16, v128
	v_and_b32_e32 v73, 0xffff0000, v128
	v_lshlrev_b32_e32 v74, 16, v129
	v_and_b32_e32 v75, 0xffff0000, v129
	v_mul_f32_e32 v0, 0xbfb8aa3b, v72
	v_mul_f32_e32 v76, 0xbfb8aa3b, v73
	v_mul_f32_e32 v77, 0xbfb8aa3b, v74
	v_mul_f32_e32 v78, 0xbfb8aa3b, v75
	v_exp_f32_e32 v0, v0
	v_exp_f32_e32 v76, v76
	v_exp_f32_e32 v77, v77
	v_exp_f32_e32 v78, v78
	v_add_f32_e32 v0, 1.0, v0
	v_add_f32_e32 v79, 1.0, v76
	v_add_f32_e32 v80, 1.0, v77
	v_add_f32_e32 v81, 1.0, v78
	v_rcp_f32_e32 v76, v0
	v_rcp_f32_e32 v77, v79
	v_rcp_f32_e32 v78, v80
	v_rcp_f32_e32 v79, v81
	v_add_lshl_u32 v0, v71, v170, 1
	v_pk_mul_f32 v[72:73], v[76:77], v[72:73]
	v_pk_mul_f32 v[74:75], v[78:79], v[74:75]
	s_waitcnt vmcnt(3)
	v_pk_mul_f32 v[62:63], v[240:241], v[62:63]
	v_pk_mul_f32 v[64:65], v[242:243], v[64:65]
	v_pk_mul_f32 v[62:63], v[72:73], v[62:63]
	v_pk_mul_f32 v[64:65], v[74:75], v[64:65]
	v_cvt_pk_bf16_f32 v62, v62, v63
	v_cvt_pk_bf16_f32 v63, v64, v65
	global_store_dwordx2 v0, v[62:63], s[24:25]
	global_load_dwordx4 v[240:243], v[92:93], off
	v_lshlrev_b32_e32 v66, 16, v126
	v_and_b32_e32 v67, 0xffff0000, v126
	v_lshlrev_b32_e32 v68, 16, v127
	v_and_b32_e32 v69, 0xffff0000, v127
	v_mul_f32_e32 v0, 0xbfb8aa3b, v66
	v_mul_f32_e32 v72, 0xbfb8aa3b, v67
	v_mul_f32_e32 v73, 0xbfb8aa3b, v68
	v_mul_f32_e32 v74, 0xbfb8aa3b, v69
	v_exp_f32_e32 v0, v0
	v_exp_f32_e32 v72, v72
	v_exp_f32_e32 v73, v73
	v_exp_f32_e32 v74, v74
	v_add_f32_e32 v0, 1.0, v0
	v_add_f32_e32 v75, 1.0, v72
	v_add_f32_e32 v76, 1.0, v73
	v_add_f32_e32 v77, 1.0, v74
	v_rcp_f32_e32 v72, v0
	v_rcp_f32_e32 v73, v75
	v_rcp_f32_e32 v74, v76
	v_rcp_f32_e32 v75, v77
	v_add_lshl_u32 v0, v71, v171, 1
	v_pk_mul_f32 v[66:67], v[72:73], v[66:67]
	v_pk_mul_f32 v[68:69], v[74:75], v[68:69]
	s_waitcnt vmcnt(4)
	v_pk_mul_f32 v[58:59], v[244:245], v[58:59]
	v_pk_mul_f32 v[60:61], v[246:247], v[60:61]
	v_pk_mul_f32 v[58:59], v[66:67], v[58:59]
	v_pk_mul_f32 v[60:61], v[68:69], v[60:61]
	v_cvt_pk_bf16_f32 v58, v58, v59
	v_cvt_pk_bf16_f32 v59, v60, v61
	global_store_dwordx2 v0, v[58:59], s[24:25]
	global_load_dwordx4 v[244:247], v[94:95], off
	v_lshlrev_b32_e32 v62, 16, v124
	v_and_b32_e32 v63, 0xffff0000, v124
	v_lshlrev_b32_e32 v64, 16, v125
	v_and_b32_e32 v65, 0xffff0000, v125
	v_mul_f32_e32 v0, 0xbfb8aa3b, v62
	v_mul_f32_e32 v66, 0xbfb8aa3b, v63
	v_mul_f32_e32 v67, 0xbfb8aa3b, v64
	v_mul_f32_e32 v68, 0xbfb8aa3b, v65
	v_exp_f32_e32 v0, v0
	v_exp_f32_e32 v66, v66
	v_exp_f32_e32 v67, v67
	v_exp_f32_e32 v68, v68
	v_add_f32_e32 v0, 1.0, v0
	v_add_f32_e32 v69, 1.0, v66
	v_add_f32_e32 v72, 1.0, v67
	v_add_f32_e32 v73, 1.0, v68
	v_rcp_f32_e32 v66, v0
	v_rcp_f32_e32 v67, v69
	v_rcp_f32_e32 v68, v72
	v_rcp_f32_e32 v69, v73
	v_add_lshl_u32 v0, v71, v172, 1
	v_pk_mul_f32 v[62:63], v[66:67], v[62:63]
	v_pk_mul_f32 v[64:65], v[68:69], v[64:65]
	s_waitcnt vmcnt(5)
	v_pk_mul_f32 v[54:55], v[54:55], v[248:249]
	v_pk_mul_f32 v[56:57], v[56:57], v[250:251]
	v_pk_mul_f32 v[54:55], v[62:63], v[54:55]
	v_pk_mul_f32 v[56:57], v[64:65], v[56:57]
	v_cvt_pk_bf16_f32 v54, v54, v55
	v_cvt_pk_bf16_f32 v55, v56, v57
	global_store_dwordx2 v0, v[54:55], s[24:25]
	global_load_dwordx4 v[248:251], v[96:97], off
	v_lshlrev_b32_e32 v58, 16, v122
	v_and_b32_e32 v59, 0xffff0000, v122
	v_lshlrev_b32_e32 v60, 16, v123
	v_and_b32_e32 v61, 0xffff0000, v123
	v_mul_f32_e32 v0, 0xbfb8aa3b, v58
	v_mul_f32_e32 v62, 0xbfb8aa3b, v59
	v_mul_f32_e32 v63, 0xbfb8aa3b, v60
	v_mul_f32_e32 v64, 0xbfb8aa3b, v61
	v_exp_f32_e32 v0, v0
	v_exp_f32_e32 v62, v62
	v_exp_f32_e32 v63, v63
	v_exp_f32_e32 v64, v64
	v_add_f32_e32 v0, 1.0, v0
	v_add_f32_e32 v65, 1.0, v62
	v_add_f32_e32 v66, 1.0, v63
	v_add_f32_e32 v67, 1.0, v64
	v_rcp_f32_e32 v62, v0
	v_rcp_f32_e32 v63, v65
	v_rcp_f32_e32 v64, v66
	v_rcp_f32_e32 v65, v67
	v_add_lshl_u32 v0, v71, v173, 1
	v_pk_mul_f32 v[58:59], v[62:63], v[58:59]
	v_pk_mul_f32 v[60:61], v[64:65], v[60:61]
	s_waitcnt vmcnt(4)
	v_pk_mul_f32 v[50:51], v[50:51], v[240:241]
	v_pk_mul_f32 v[52:53], v[52:53], v[242:243]
	v_pk_mul_f32 v[50:51], v[58:59], v[50:51]
	v_pk_mul_f32 v[52:53], v[60:61], v[52:53]
	v_cvt_pk_bf16_f32 v50, v50, v51
	v_cvt_pk_bf16_f32 v51, v52, v53
	global_store_dwordx2 v0, v[50:51], s[24:25]
	global_load_dwordx4 v[240:243], v[98:99], off
	v_lshlrev_b32_e32 v54, 16, v120
	v_and_b32_e32 v55, 0xffff0000, v120
	v_lshlrev_b32_e32 v56, 16, v121
	v_and_b32_e32 v57, 0xffff0000, v121
	v_mul_f32_e32 v0, 0xbfb8aa3b, v54
	v_mul_f32_e32 v58, 0xbfb8aa3b, v55
	v_mul_f32_e32 v59, 0xbfb8aa3b, v56
	v_mul_f32_e32 v60, 0xbfb8aa3b, v57
	v_exp_f32_e32 v0, v0
	v_exp_f32_e32 v58, v58
	v_exp_f32_e32 v59, v59
	v_exp_f32_e32 v60, v60
	v_add_f32_e32 v0, 1.0, v0
	v_add_f32_e32 v61, 1.0, v58
	v_add_f32_e32 v62, 1.0, v59
	v_add_f32_e32 v63, 1.0, v60
	v_rcp_f32_e32 v58, v0
	v_rcp_f32_e32 v59, v61
	v_rcp_f32_e32 v60, v62
	v_rcp_f32_e32 v61, v63
	v_add_lshl_u32 v0, v71, v174, 1
	v_pk_mul_f32 v[54:55], v[58:59], v[54:55]
	v_pk_mul_f32 v[56:57], v[60:61], v[56:57]
	s_waitcnt vmcnt(4)
	v_pk_mul_f32 v[46:47], v[46:47], v[244:245]
	v_pk_mul_f32 v[48:49], v[48:49], v[246:247]
	v_pk_mul_f32 v[46:47], v[54:55], v[46:47]
	v_pk_mul_f32 v[48:49], v[56:57], v[48:49]
	v_cvt_pk_bf16_f32 v46, v46, v47
	v_cvt_pk_bf16_f32 v47, v48, v49
	global_store_dwordx2 v0, v[46:47], s[24:25]
	v_lshlrev_b32_e32 v50, 16, v118
	v_and_b32_e32 v51, 0xffff0000, v118
	v_lshlrev_b32_e32 v52, 16, v119
	v_and_b32_e32 v53, 0xffff0000, v119
	v_mul_f32_e32 v0, 0xbfb8aa3b, v50
	v_mul_f32_e32 v54, 0xbfb8aa3b, v51
	v_mul_f32_e32 v55, 0xbfb8aa3b, v52
	v_mul_f32_e32 v56, 0xbfb8aa3b, v53
	v_exp_f32_e32 v0, v0
	v_exp_f32_e32 v54, v54
	v_exp_f32_e32 v55, v55
	v_exp_f32_e32 v56, v56
	v_add_f32_e32 v0, 1.0, v0
	v_add_f32_e32 v57, 1.0, v54
	v_add_f32_e32 v58, 1.0, v55
	v_add_f32_e32 v59, 1.0, v56
	v_rcp_f32_e32 v54, v0
	v_rcp_f32_e32 v55, v57
	v_rcp_f32_e32 v56, v58
	v_rcp_f32_e32 v57, v59
	v_add_lshl_u32 v0, v71, v175, 1
	v_pk_mul_f32 v[50:51], v[54:55], v[50:51]
	v_add_lshl_u32 v54, v71, v176, 1
	v_pk_mul_f32 v[52:53], v[56:57], v[52:53]
	s_waitcnt vmcnt(3)
	v_pk_mul_f32 v[42:43], v[42:43], v[248:249]
	v_pk_mul_f32 v[44:45], v[44:45], v[250:251]
	v_pk_mul_f32 v[42:43], v[50:51], v[42:43]
	v_pk_mul_f32 v[44:45], v[52:53], v[44:45]
	v_cvt_pk_bf16_f32 v42, v42, v43
	v_cvt_pk_bf16_f32 v43, v44, v45
	global_store_dwordx2 v0, v[42:43], s[24:25]
	v_lshlrev_b32_e32 v46, 16, v116
	v_and_b32_e32 v47, 0xffff0000, v116
	v_lshlrev_b32_e32 v48, 16, v117
	v_and_b32_e32 v49, 0xffff0000, v117
	v_mul_f32_e32 v0, 0xbfb8aa3b, v46
	v_mul_f32_e32 v50, 0xbfb8aa3b, v47
	v_mul_f32_e32 v51, 0xbfb8aa3b, v48
	v_mul_f32_e32 v52, 0xbfb8aa3b, v49
	v_exp_f32_e32 v0, v0
	v_exp_f32_e32 v50, v50
	v_exp_f32_e32 v51, v51
	v_exp_f32_e32 v52, v52
	v_add_f32_e32 v0, 1.0, v0
	v_add_f32_e32 v53, 1.0, v50
	v_add_f32_e32 v55, 1.0, v51
	v_add_f32_e32 v56, 1.0, v52
	v_rcp_f32_e32 v50, v0
	v_rcp_f32_e32 v51, v53
	v_rcp_f32_e32 v52, v55
	v_rcp_f32_e32 v53, v56
	v_pk_mul_f32 v[46:47], v[50:51], v[46:47]
	v_pk_mul_f32 v[48:49], v[52:53], v[48:49]
	s_waitcnt vmcnt(2)
	v_pk_mul_f32 v[38:39], v[38:39], v[240:241]
	v_pk_mul_f32 v[40:41], v[40:41], v[242:243]
	v_pk_mul_f32 v[38:39], v[46:47], v[38:39]
	v_pk_mul_f32 v[40:41], v[48:49], v[40:41]
	v_cvt_pk_bf16_f32 v38, v38, v39
	v_cvt_pk_bf16_f32 v39, v40, v41
	global_store_dwordx2 v54, v[38:39], s[24:25]
	s_barrier
	s_cbranch_vccz .LBB0_912
